# v55 + s_setprio 3 while a wave runs the tier-1 re-check loop, s_setprio 0 afterwards
# speedup vs baseline: 1.0142x; 1.0043x over previous
.LBB1_10:
	s_or_b64 exec, exec, s[0:1]
	v_add_f32_e32 v6, v6, v7
	v_add_f32_e32 v7, v8, v9
	v_add_f32_e32 v2, v2, v3
	v_add_f32_e32 v3, v4, v5
	v_add_f32_e32 v6, v6, v7
	v_add_f32_e32 v2, v2, v3
	v_add_f32_e32 v2, v6, v2
	v_mul_f32_e32 v2, 0x36800000, v2
	s_mov_b32 s3, 0xf800000
	v_mul_f32_e32 v3, 0x4f800000, v2
	v_cmp_gt_f32_e32 vcc, s3, v2
	v_add_f32_e32 v4, v133, v134
	v_add_f32_e32 v5, v135, v136
	v_cndmask_b32_e32 v2, v2, v3, vcc
	v_sqrt_f32_e32 v3, v2
	v_cndmask_b32_e64 v4, v5, v4, s[4:5]
	v_mov_b32_e32 v23, 0x260
	v_and_b32_e32 v17, 0x7fffffff, v12
	v_add_u32_e32 v5, -1, v3
	v_fma_f32 v6, -v5, v3, v2
	v_cmp_ge_f32_e64 s[0:1], 0, v6
	v_add_u32_e32 v6, 1, v3
	v_and_b32_e32 v22, 0x3ff, v12
	v_cndmask_b32_e64 v5, v3, v5, s[0:1]
	v_fma_f32 v3, -v6, v3, v2
	v_cmp_lt_f32_e64 s[0:1], 0, v3
	s_brev_b32 s33, -2
	s_nop 0
	v_cndmask_b32_e64 v3, v5, v6, s[0:1]
	v_mul_f32_e32 v5, 0x37800000, v3
	v_cndmask_b32_e32 v3, v3, v5, vcc
	v_mul_f32_e32 v5, 0x4f800000, v4
	v_cmp_gt_f32_e32 vcc, s3, v4
	v_cmp_class_f32_e64 s[0:1], v2, v23
	s_nop 0
	v_cndmask_b32_e32 v4, v4, v5, vcc
	v_sqrt_f32_e32 v5, v4
	v_cndmask_b32_e64 v3, v3, v2, s[0:1]
	v_cndmask_b32_e64 v2, v16, v13, s[4:5]
	v_add_u32_e32 v6, -1, v5
	v_fma_f32 v7, -v6, v5, v4
	v_cmp_ge_f32_e64 s[0:1], 0, v7
	v_add_u32_e32 v7, 1, v5
	s_nop 0
	v_cndmask_b32_e64 v6, v5, v6, s[0:1]
	v_fma_f32 v5, -v7, v5, v4
	v_cmp_lt_f32_e64 s[0:1], 0, v5
	s_nop 1
	v_cndmask_b32_e64 v5, v6, v7, s[0:1]
	v_mul_f32_e32 v6, 0x37800000, v5
	v_cndmask_b32_e32 v5, v5, v6, vcc
	v_cmp_class_f32_e32 vcc, v4, v23
	s_mov_b32 s0, 0x3b51b717
	s_mov_b32 s1, 0x39800000
	v_cndmask_b32_e32 v4, v5, v4, vcc
	v_mul_f32_e32 v16, v3, v4
	v_pk_mul_f32 v[4:5], v[16:17], s[0:1]
	s_nop 0
	v_add_f32_e32 v3, v4, v5
	v_add_f32_e32 v3, 0x358637bd, v3
	v_sub_f32_e32 v4, v2, v12
	v_cmp_lt_f32_e32 vcc, v4, v3
	s_and_b64 s[8:9], s[6:7], vcc
	s_cbranch_scc0 .LBB1_51
	s_setprio 3
	v_cndmask_b32_e64 v4, v11, v10, s[4:5]
	v_and_b32_e32 v17, 0x3ff, v2
	v_and_b32_e32 v2, 0x3ff, v4
	v_sub_f32_e32 v4, v4, v12
	v_cmp_lt_f32_e32 vcc, v4, v3
	v_add_u32_e32 v6, 0x19060, v130
	v_mov_b32_e32 v131, 0
	v_cndmask_b32_e32 v24, -1, v2, vcc
	v_add_u32_e32 v2, 0x19460, v130
	ds_read_b128 v[2:5], v2
	ds_read_b128 v[6:9], v6
	v_lshl_add_u64 v[18:19], s[20:21], 0, v[130:131]
	v_lshl_add_u64 v[20:21], s[36:37], 0, v[130:131]
	v_mov_b32_e32 v25, 0x3727c5ac
	s_mov_b32 s5, 0
	s_mov_b32 s34, 0x378e98ab
	s_mov_b32 s35, 0x3b7cd369
	s_mov_b32 s36, 0xbcc618b2
	s_mov_b32 s37, 0x3dda74e4
	s_mov_b32 s40, 0x3f228afd
	s_mov_b32 s41, 0x3e03c728
	s_mov_b32 s42, 0xbfb8aa3b
	s_mov_b32 s43, 0x42ce8ed0
	s_mov_b32 s44, 0xc2b17218
	v_mov_b32_e32 v26, 0x3ba10414
	v_mov_b32_e32 v27, 0x33d6bf95
	v_mov_b32_e32 v28, 0x3851b717
	v_mov_b32_e32 v29, 0xb9c68948
	v_mov_b32_e32 v30, 0x7f800000
	s_branch .LBB1_15

.LBB1_51:
	s_setprio 0
	s_and_saveexec_b64 s[0:1], s[6:7]
	s_cbranch_execz .LBB1_53
	v_or_b32_e32 v2, v128, v129
	v_ashrrev_i32_e32 v3, 31, v2
	v_cvt_f32_i32_e32 v4, v22
	v_lshl_add_u64 v[2:3], v[2:3], 2, s[14:15]
	v_add_co_u32_e32 v2, vcc, 0x4000000, v2
	s_nop 1
	v_addc_co_u32_e32 v3, vcc, 0, v3, vcc
	global_store_dword v[2:3], v4, off
